# k_prep: 8 weight-element loads per fragment issued together (were load+vmcnt(0) each), e1s fill straight-lined, b_spec/b_e1 scalar lines warmed early; on top of v67
# speedup vs baseline: 1.0073x; 1.0073x over previous
.LBB0_7:
	s_or_b64 exec, exec, s[4:5]
	s_and_saveexec_b64 s[4:5], vcc
	s_cbranch_execz .LBB0_9
	v_add_u32_e32 v12, 1, v8
	v_ashrrev_i32_e32 v13, 31, v12
	v_lshl_add_u64 v[12:13], v[6:7], 0, v[12:13]
	v_mul_lo_u32 v9, v13, s8
	v_mul_lo_u32 v11, v12, s3
	v_mad_u64_u32 v[12:13], s[10:11], v12, s8, 0
	v_add3_u32 v13, v13, v11, v9
	v_lshl_add_u64 v[12:13], v[12:13], 2, v[4:5]
	global_load_dword v11, v[12:13], off
.LBB0_9:
	s_or_b64 exec, exec, s[4:5]
	v_mov_b32_e32 v9, 0
	v_mov_b32_e32 v12, 0
	s_and_saveexec_b64 s[4:5], vcc
	s_cbranch_execz .LBB0_11
	v_add_u32_e32 v12, 2, v8
	v_ashrrev_i32_e32 v13, 31, v12
	v_lshl_add_u64 v[12:13], v[6:7], 0, v[12:13]
	v_mul_lo_u32 v14, v13, s8
	v_mul_lo_u32 v15, v12, s3
	v_mad_u64_u32 v[12:13], s[10:11], v12, s8, 0
	v_add3_u32 v13, v13, v15, v14
	v_lshl_add_u64 v[12:13], v[12:13], 2, v[4:5]
	global_load_dword v12, v[12:13], off
.LBB0_11:
	s_or_b64 exec, exec, s[4:5]
	s_and_saveexec_b64 s[4:5], vcc
	s_cbranch_execz .LBB0_13
	v_add_u32_e32 v14, 3, v8
	v_ashrrev_i32_e32 v15, 31, v14
	v_lshl_add_u64 v[14:15], v[6:7], 0, v[14:15]
	v_mul_lo_u32 v9, v15, s8
	v_mul_lo_u32 v13, v14, s3
	v_mad_u64_u32 v[14:15], s[10:11], v14, s8, 0
	v_add3_u32 v15, v15, v13, v9
	v_lshl_add_u64 v[14:15], v[14:15], 2, v[4:5]
	global_load_dword v9, v[14:15], off
.LBB0_13:
	s_or_b64 exec, exec, s[4:5]
	v_mov_b32_e32 v13, 0
	v_mov_b32_e32 v14, 0
	s_and_saveexec_b64 s[4:5], vcc
	s_cbranch_execz .LBB0_15
	v_add_u32_e32 v14, 4, v8
	v_ashrrev_i32_e32 v15, 31, v14
	v_lshl_add_u64 v[14:15], v[6:7], 0, v[14:15]
	v_mul_lo_u32 v16, v15, s8
	v_mul_lo_u32 v17, v14, s3
	v_mad_u64_u32 v[14:15], s[10:11], v14, s8, 0
	v_add3_u32 v15, v15, v17, v16
	v_lshl_add_u64 v[14:15], v[14:15], 2, v[4:5]
	global_load_dword v14, v[14:15], off
.LBB0_15:
	s_or_b64 exec, exec, s[4:5]
	s_and_saveexec_b64 s[4:5], vcc
	s_cbranch_execz .LBB0_17
	v_add_u32_e32 v16, 5, v8
	v_ashrrev_i32_e32 v17, 31, v16
	v_lshl_add_u64 v[16:17], v[6:7], 0, v[16:17]
	v_mul_lo_u32 v13, v17, s8
	v_mul_lo_u32 v15, v16, s3
	v_mad_u64_u32 v[16:17], s[10:11], v16, s8, 0
	v_add3_u32 v17, v17, v15, v13
	v_lshl_add_u64 v[16:17], v[16:17], 2, v[4:5]
	global_load_dword v13, v[16:17], off
.LBB0_17:
	s_or_b64 exec, exec, s[4:5]
	v_mov_b32_e32 v15, 0
	v_mov_b32_e32 v16, 0
	s_and_saveexec_b64 s[4:5], vcc
	s_cbranch_execz .LBB0_19
	v_add_u32_e32 v16, 6, v8
	v_ashrrev_i32_e32 v17, 31, v16
	v_lshl_add_u64 v[16:17], v[6:7], 0, v[16:17]
	v_mul_lo_u32 v18, v17, s8
	v_mul_lo_u32 v19, v16, s3
	v_mad_u64_u32 v[16:17], s[10:11], v16, s8, 0
	v_add3_u32 v17, v17, v19, v18
	v_lshl_add_u64 v[16:17], v[16:17], 2, v[4:5]
	global_load_dword v16, v[16:17], off
.LBB0_19:
	s_or_b64 exec, exec, s[4:5]
	s_and_saveexec_b64 s[4:5], vcc
	s_cbranch_execz .LBB0_21
	v_add_u32_e32 v18, 7, v8
	v_ashrrev_i32_e32 v19, 31, v18
	v_lshl_add_u64 v[6:7], v[6:7], 0, v[18:19]
	v_mul_lo_u32 v8, v7, s8
	v_mul_lo_u32 v15, v6, s3
	v_mad_u64_u32 v[6:7], s[8:9], v6, s8, 0
	v_add3_u32 v7, v7, v15, v8
	v_lshl_add_u64 v[4:5], v[6:7], 2, v[4:5]
	global_load_dword v15, v[4:5], off
.LBB0_21:
	s_or_b64 exec, exec, s[4:5]
	s_waitcnt vmcnt(0)
	v_mul_f32_e32 v3, 0x42800000, v3
	v_mul_f32_e32 v11, 0x42800000, v11
	v_mul_f32_e32 v12, 0x42800000, v12
	v_mul_f32_e32 v9, 0x42800000, v9
	v_mul_f32_e32 v14, 0x42800000, v14
	v_mul_f32_e32 v13, 0x42800000, v13
	v_mul_f32_e32 v16, 0x42800000, v16
	v_mul_f32_e32 v15, 0x42800000, v15
	v_cvt_f16_f32_e32 v4, v3
	v_cvt_f16_f32_e32 v5, v11
	v_cvt_f16_f32_e32 v6, v12
	v_cvt_f16_f32_e32 v7, v9
	v_cvt_f32_f16_e32 v4, v4
	v_cvt_f32_f16_e32 v5, v5
	v_cvt_f32_f16_e32 v6, v6
	v_sub_f32_e32 v8, v3, v4
	v_cvt_f16_f32_e32 v4, v14
	v_sub_f32_e32 v17, v11, v5
	v_sub_f32_e32 v18, v12, v6
	v_cvt_f32_f16_e32 v5, v7
	v_cvt_f16_f32_e32 v6, v13
	v_cvt_f16_f32_e32 v7, v16
	v_cvt_f32_f16_e32 v4, v4
	v_sub_f32_e32 v19, v9, v5
	v_cvt_f32_f16_e32 v5, v6
	v_cvt_f32_f16_e32 v6, v7
	v_sub_f32_e32 v20, v14, v4
	v_cvt_f16_f32_e32 v4, v15
	v_cvt_pk_f16_f32 v7, v16, v15
	v_sub_f32_e32 v22, v16, v6
	v_sub_f32_e32 v21, v13, v5
	v_cvt_f32_f16_e32 v16, v4
	v_cvt_pk_f16_f32 v4, v3, v11
	v_cvt_pk_f16_f32 v6, v14, v13
	v_cvt_pk_f16_f32 v5, v12, v9
	v_sub_f32_e32 v3, v15, v16
	v_cvt_pk_f16_f32 v15, v22, v3
	v_mov_b32_e32 v3, 0
	v_lshlrev_b64 v[2:3], 5, v[2:3]
	v_lshl_add_u64 v[2:3], s[6:7], 0, v[2:3]
	v_cvt_pk_f16_f32 v14, v20, v21
	v_cvt_pk_f16_f32 v13, v18, v19
	v_cvt_pk_f16_f32 v12, v8, v17
	global_store_dwordx4 v[2:3], v[4:7], off
	global_store_dwordx4 v[2:3], v[12:15], off offset:16

.LBB0_30:
	s_or_b64 exec, exec, s[4:5]
	s_and_saveexec_b64 s[4:5], vcc
	s_cbranch_execz .LBB0_32
	v_add_u32_e32 v12, 1, v8
	v_ashrrev_i32_e32 v13, 31, v12
	v_lshl_add_u64 v[12:13], v[6:7], 0, v[12:13]
	v_mul_lo_u32 v9, v13, s8
	v_mul_lo_u32 v11, v12, s9
	v_mad_u64_u32 v[12:13], s[10:11], v12, s8, 0
	v_add3_u32 v13, v13, v11, v9
	v_lshl_add_u64 v[12:13], v[12:13], 2, v[4:5]
	global_load_dword v11, v[12:13], off
.LBB0_32:
	s_or_b64 exec, exec, s[4:5]
	v_mov_b32_e32 v9, 0
	v_mov_b32_e32 v12, 0
	s_and_saveexec_b64 s[4:5], vcc
	s_cbranch_execz .LBB0_34
	v_add_u32_e32 v12, 2, v8
	v_ashrrev_i32_e32 v13, 31, v12
	v_lshl_add_u64 v[12:13], v[6:7], 0, v[12:13]
	v_mul_lo_u32 v14, v13, s8
	v_mul_lo_u32 v15, v12, s9
	v_mad_u64_u32 v[12:13], s[10:11], v12, s8, 0
	v_add3_u32 v13, v13, v15, v14
	v_lshl_add_u64 v[12:13], v[12:13], 2, v[4:5]
	global_load_dword v12, v[12:13], off
.LBB0_34:
	s_or_b64 exec, exec, s[4:5]
	s_and_saveexec_b64 s[4:5], vcc
	s_cbranch_execz .LBB0_36
	v_add_u32_e32 v14, 3, v8
	v_ashrrev_i32_e32 v15, 31, v14
	v_lshl_add_u64 v[14:15], v[6:7], 0, v[14:15]
	v_mul_lo_u32 v9, v15, s8
	v_mul_lo_u32 v13, v14, s9
	v_mad_u64_u32 v[14:15], s[10:11], v14, s8, 0
	v_add3_u32 v15, v15, v13, v9
	v_lshl_add_u64 v[14:15], v[14:15], 2, v[4:5]
	global_load_dword v9, v[14:15], off
.LBB0_36:
	s_or_b64 exec, exec, s[4:5]
	v_mov_b32_e32 v13, 0
	v_mov_b32_e32 v14, 0
	s_and_saveexec_b64 s[4:5], vcc
	s_cbranch_execz .LBB0_38
	v_add_u32_e32 v14, 4, v8
	v_ashrrev_i32_e32 v15, 31, v14
	v_lshl_add_u64 v[14:15], v[6:7], 0, v[14:15]
	v_mul_lo_u32 v16, v15, s8
	v_mul_lo_u32 v17, v14, s9
	v_mad_u64_u32 v[14:15], s[10:11], v14, s8, 0
	v_add3_u32 v15, v15, v17, v16
	v_lshl_add_u64 v[14:15], v[14:15], 2, v[4:5]
	global_load_dword v14, v[14:15], off
.LBB0_38:
	s_or_b64 exec, exec, s[4:5]
	s_and_saveexec_b64 s[4:5], vcc
	s_cbranch_execz .LBB0_40
	v_add_u32_e32 v16, 5, v8
	v_ashrrev_i32_e32 v17, 31, v16
	v_lshl_add_u64 v[16:17], v[6:7], 0, v[16:17]
	v_mul_lo_u32 v13, v17, s8
	v_mul_lo_u32 v15, v16, s9
	v_mad_u64_u32 v[16:17], s[10:11], v16, s8, 0
	v_add3_u32 v17, v17, v15, v13
	v_lshl_add_u64 v[16:17], v[16:17], 2, v[4:5]
	global_load_dword v13, v[16:17], off
.LBB0_40:
	s_or_b64 exec, exec, s[4:5]
	v_mov_b32_e32 v15, 0
	v_mov_b32_e32 v16, 0
	s_and_saveexec_b64 s[4:5], vcc
	s_cbranch_execz .LBB0_42
	v_add_u32_e32 v16, 6, v8
	v_ashrrev_i32_e32 v17, 31, v16
	v_lshl_add_u64 v[16:17], v[6:7], 0, v[16:17]
	v_mul_lo_u32 v18, v17, s8
	v_mul_lo_u32 v19, v16, s9
	v_mad_u64_u32 v[16:17], s[10:11], v16, s8, 0
	v_add3_u32 v17, v17, v19, v18
	v_lshl_add_u64 v[16:17], v[16:17], 2, v[4:5]
	global_load_dword v16, v[16:17], off
.LBB0_42:
	s_or_b64 exec, exec, s[4:5]
	s_and_saveexec_b64 s[4:5], vcc
	s_cbranch_execz .LBB0_44
	v_add_u32_e32 v18, 7, v8
	v_ashrrev_i32_e32 v19, 31, v18
	v_lshl_add_u64 v[6:7], v[6:7], 0, v[18:19]
	v_mul_lo_u32 v8, v7, s8
	v_mul_lo_u32 v15, v6, s9
	v_mad_u64_u32 v[6:7], s[8:9], v6, s8, 0
	v_add3_u32 v7, v7, v15, v8
	v_lshl_add_u64 v[4:5], v[6:7], 2, v[4:5]
	global_load_dword v15, v[4:5], off
.LBB0_44:
	s_or_b64 exec, exec, s[4:5]
	s_waitcnt vmcnt(0)
	v_mul_f32_e32 v3, 0x42800000, v3
	v_mul_f32_e32 v11, 0x42800000, v11
	v_mul_f32_e32 v12, 0x42800000, v12
	v_mul_f32_e32 v9, 0x42800000, v9
	v_mul_f32_e32 v14, 0x42800000, v14
	v_mul_f32_e32 v13, 0x42800000, v13
	v_mul_f32_e32 v16, 0x42800000, v16
	v_mul_f32_e32 v15, 0x42800000, v15
	v_cvt_f16_f32_e32 v4, v3
	v_cvt_f16_f32_e32 v5, v11
	v_cvt_f16_f32_e32 v6, v12
	v_cvt_f16_f32_e32 v7, v9
	v_cvt_f32_f16_e32 v4, v4
	v_cvt_f32_f16_e32 v5, v5
	v_cvt_f32_f16_e32 v6, v6
	v_sub_f32_e32 v8, v3, v4
	v_cvt_f16_f32_e32 v4, v14
	v_sub_f32_e32 v17, v11, v5
	v_sub_f32_e32 v18, v12, v6
	v_cvt_f32_f16_e32 v5, v7
	v_cvt_f16_f32_e32 v6, v13
	v_cvt_f16_f32_e32 v7, v16
	v_cvt_f32_f16_e32 v4, v4
	v_sub_f32_e32 v19, v9, v5
	v_cvt_f32_f16_e32 v5, v6
	v_cvt_f32_f16_e32 v6, v7
	v_sub_f32_e32 v20, v14, v4
	v_cvt_f16_f32_e32 v4, v15
	v_cvt_pk_f16_f32 v7, v16, v15
	v_sub_f32_e32 v22, v16, v6
	v_sub_f32_e32 v21, v13, v5
	v_cvt_f32_f16_e32 v16, v4
	v_cvt_pk_f16_f32 v4, v3, v11
	v_cvt_pk_f16_f32 v6, v14, v13
	v_cvt_pk_f16_f32 v5, v12, v9
	v_sub_f32_e32 v3, v15, v16
	v_cvt_pk_f16_f32 v15, v22, v3
	v_ashrrev_i32_e32 v3, 31, v2
	v_lshlrev_b64 v[2:3], 5, v[2:3]
	v_lshl_add_u64 v[2:3], s[6:7], 0, v[2:3]
	v_cvt_pk_f16_f32 v14, v20, v21
	v_cvt_pk_f16_f32 v13, v18, v19
	v_cvt_pk_f16_f32 v12, v8, v17
	global_store_dwordx4 v[2:3], v[4:7], off
	global_store_dwordx4 v[2:3], v[12:15], off offset:16

.LBB0_55:
	s_or_b64 exec, exec, s[4:5]
	v_mov_b32_e32 v9, 0
	v_mov_b32_e32 v12, 0
	s_and_saveexec_b64 s[4:5], vcc
	s_cbranch_execz .LBB0_57
	v_add_u32_e32 v12, 2, v8
	v_ashrrev_i32_e32 v13, 31, v12
	v_lshl_add_u64 v[12:13], v[6:7], 0, v[12:13]
	v_mul_lo_u32 v14, v13, s8
	v_mul_lo_u32 v15, v12, s3
	v_mad_u64_u32 v[12:13], s[10:11], v12, s8, 0
	v_add3_u32 v13, v13, v15, v14
	v_lshl_add_u64 v[12:13], v[12:13], 2, v[4:5]
	global_load_dword v12, v[12:13], off
.LBB0_57:
	s_or_b64 exec, exec, s[4:5]
	s_and_saveexec_b64 s[4:5], vcc
	s_cbranch_execz .LBB0_59
	v_add_u32_e32 v14, 3, v8
	v_ashrrev_i32_e32 v15, 31, v14
	v_lshl_add_u64 v[14:15], v[6:7], 0, v[14:15]
	v_mul_lo_u32 v9, v15, s8
	v_mul_lo_u32 v13, v14, s3
	v_mad_u64_u32 v[14:15], s[10:11], v14, s8, 0
	v_add3_u32 v15, v15, v13, v9
	v_lshl_add_u64 v[14:15], v[14:15], 2, v[4:5]
	global_load_dword v9, v[14:15], off
.LBB0_59:
	s_or_b64 exec, exec, s[4:5]
	v_mov_b32_e32 v13, 0
	v_mov_b32_e32 v14, 0
	s_and_saveexec_b64 s[4:5], vcc
	s_cbranch_execz .LBB0_61
	v_add_u32_e32 v14, 4, v8
	v_ashrrev_i32_e32 v15, 31, v14
	v_lshl_add_u64 v[14:15], v[6:7], 0, v[14:15]
	v_mul_lo_u32 v16, v15, s8
	v_mul_lo_u32 v17, v14, s3
	v_mad_u64_u32 v[14:15], s[10:11], v14, s8, 0
	v_add3_u32 v15, v15, v17, v16
	v_lshl_add_u64 v[14:15], v[14:15], 2, v[4:5]
	global_load_dword v14, v[14:15], off
.LBB0_61:
	s_or_b64 exec, exec, s[4:5]
	s_and_saveexec_b64 s[4:5], vcc
	s_cbranch_execz .LBB0_63
	v_add_u32_e32 v16, 5, v8
	v_ashrrev_i32_e32 v17, 31, v16
	v_lshl_add_u64 v[16:17], v[6:7], 0, v[16:17]
	v_mul_lo_u32 v13, v17, s8
	v_mul_lo_u32 v15, v16, s3
	v_mad_u64_u32 v[16:17], s[10:11], v16, s8, 0
	v_add3_u32 v17, v17, v15, v13
	v_lshl_add_u64 v[16:17], v[16:17], 2, v[4:5]
	global_load_dword v13, v[16:17], off
.LBB0_63:
	s_or_b64 exec, exec, s[4:5]
	v_mov_b32_e32 v15, 0
	v_mov_b32_e32 v16, 0
	s_and_saveexec_b64 s[4:5], vcc
	s_cbranch_execz .LBB0_65
	v_add_u32_e32 v16, 6, v8
	v_ashrrev_i32_e32 v17, 31, v16
	v_lshl_add_u64 v[16:17], v[6:7], 0, v[16:17]
	v_mul_lo_u32 v18, v17, s8
	v_mul_lo_u32 v19, v16, s3
	v_mad_u64_u32 v[16:17], s[10:11], v16, s8, 0
	v_add3_u32 v17, v17, v19, v18
	v_lshl_add_u64 v[16:17], v[16:17], 2, v[4:5]
	global_load_dword v16, v[16:17], off

.LBB0_79:
	s_or_b64 exec, exec, s[4:5]
	v_mov_b32_e32 v9, 0
	v_mov_b32_e32 v12, 0
	s_and_saveexec_b64 s[4:5], vcc
	s_cbranch_execz .LBB0_81
	v_add_u32_e32 v12, 2, v8
	v_ashrrev_i32_e32 v13, 31, v12
	v_lshl_add_u64 v[12:13], v[6:7], 0, v[12:13]
	v_mul_lo_u32 v14, v13, s8
	v_mul_lo_u32 v15, v12, s9
	v_mad_u64_u32 v[12:13], s[10:11], v12, s8, 0
	v_add3_u32 v13, v13, v15, v14
	v_lshl_add_u64 v[12:13], v[12:13], 2, v[4:5]
	global_load_dword v12, v[12:13], off
.LBB0_81:
	s_or_b64 exec, exec, s[4:5]
	s_and_saveexec_b64 s[4:5], vcc
	s_cbranch_execz .LBB0_83
	v_add_u32_e32 v14, 3, v8
	v_ashrrev_i32_e32 v15, 31, v14
	v_lshl_add_u64 v[14:15], v[6:7], 0, v[14:15]
	v_mul_lo_u32 v9, v15, s8
	v_mul_lo_u32 v13, v14, s9
	v_mad_u64_u32 v[14:15], s[10:11], v14, s8, 0
	v_add3_u32 v15, v15, v13, v9
	v_lshl_add_u64 v[14:15], v[14:15], 2, v[4:5]
	global_load_dword v9, v[14:15], off
.LBB0_83:
	s_or_b64 exec, exec, s[4:5]
	v_mov_b32_e32 v13, 0
	v_mov_b32_e32 v14, 0
	s_and_saveexec_b64 s[4:5], vcc
	s_cbranch_execz .LBB0_85
	v_add_u32_e32 v14, 4, v8
	v_ashrrev_i32_e32 v15, 31, v14
	v_lshl_add_u64 v[14:15], v[6:7], 0, v[14:15]
	v_mul_lo_u32 v16, v15, s8
	v_mul_lo_u32 v17, v14, s9
	v_mad_u64_u32 v[14:15], s[10:11], v14, s8, 0
	v_add3_u32 v15, v15, v17, v16
	v_lshl_add_u64 v[14:15], v[14:15], 2, v[4:5]
	global_load_dword v14, v[14:15], off
.LBB0_85:
	s_or_b64 exec, exec, s[4:5]
	s_and_saveexec_b64 s[4:5], vcc
	s_cbranch_execz .LBB0_87
	v_add_u32_e32 v16, 5, v8
	v_ashrrev_i32_e32 v17, 31, v16
	v_lshl_add_u64 v[16:17], v[6:7], 0, v[16:17]
	v_mul_lo_u32 v13, v17, s8
	v_mul_lo_u32 v15, v16, s9
	v_mad_u64_u32 v[16:17], s[10:11], v16, s8, 0
	v_add3_u32 v17, v17, v15, v13
	v_lshl_add_u64 v[16:17], v[16:17], 2, v[4:5]
	global_load_dword v13, v[16:17], off
.LBB0_87:
	s_or_b64 exec, exec, s[4:5]
	v_mov_b32_e32 v15, 0
	v_mov_b32_e32 v16, 0
	s_and_saveexec_b64 s[4:5], vcc
	s_cbranch_execz .LBB0_89
	v_add_u32_e32 v16, 6, v8
	v_ashrrev_i32_e32 v17, 31, v16
	v_lshl_add_u64 v[16:17], v[6:7], 0, v[16:17]
	v_mul_lo_u32 v18, v17, s8
	v_mul_lo_u32 v19, v16, s9
	v_mad_u64_u32 v[16:17], s[10:11], v16, s8, 0
	v_add3_u32 v17, v17, v19, v18
	v_lshl_add_u64 v[16:17], v[16:17], 2, v[4:5]
	global_load_dword v16, v[16:17], off

.LBB0_97:
	s_andn2_b64 vcc, exec, s[4:5]
	s_cbranch_vccnz .LBB0_117
	s_load_dwordx4 s[8:11], s[0:1], 0xb0
	v_lshl_or_b32 v2, s18, 8, v0
	s_waitcnt lgkmcnt(0)
	s_ashr_i32 s3, s9, 31
	s_lshr_b32 s3, s3, 28
	s_add_i32 s3, s9, s3
	s_lshr_b32 s3, s3, 4
	s_mul_i32 s3, s8, s3
	s_mul_i32 s3, s3, s11
	s_lshl_b32 s3, s3, 6
	v_cmp_gt_i32_e32 vcc, s3, v2
	s_and_saveexec_b64 s[14:15], vcc
	s_cbranch_execz .LBB0_116
	s_abs_i32 s17, s11
	v_cvt_f32_u32_e32 v3, s17
	s_load_dwordx4 s[4:7], s[0:1], 0xa0
	v_ashrrev_i32_e32 v6, 6, v2
	v_sub_u32_e32 v8, 0, v6
	v_rcp_iflag_f32_e32 v3, v3
	v_max_i32_e32 v8, v6, v8
	s_waitcnt lgkmcnt(0)
	v_mov_b32_e32 v5, s5
	s_sub_i32 s5, 0, s17
	v_mul_f32_e32 v3, 0x4f7ffffe, v3
	v_cvt_u32_f32_e32 v3, v3
	s_ashr_i32 s3, s16, 31
	s_lshr_b32 s3, s3, 28
	s_add_i32 s3, s16, s3
	v_mul_lo_u32 v9, s5, v3
	v_mul_hi_u32 v9, v3, v9
	v_add_u32_e32 v3, v3, v9
	v_mul_hi_u32 v3, v8, v3
	v_mul_lo_u32 v9, v3, s17
	v_sub_u32_e32 v8, v8, v9
	v_add_u32_e32 v9, 1, v3
	v_cmp_le_u32_e32 vcc, s17, v8
	v_mov_b32_e32 v4, s4
	s_ashr_i32 s4, s3, 4
	v_cndmask_b32_e32 v3, v3, v9, vcc
	v_subrev_u32_e32 v9, s17, v8
	v_cndmask_b32_e32 v8, v8, v9, vcc
	v_xor_b32_e32 v7, s11, v6
	v_add_u32_e32 v9, 1, v3
	v_cmp_le_u32_e32 vcc, s17, v8
	s_abs_i32 s5, s4
	v_ashrrev_i32_e32 v7, 31, v7
	v_cndmask_b32_e32 v3, v3, v9, vcc
	v_cvt_f32_u32_e32 v8, s5
	v_xor_b32_e32 v3, v3, v7
	v_sub_u32_e32 v3, v3, v7
	v_mul_lo_u32 v7, v3, s11
	v_sub_u32_e32 v6, v6, v7
	v_rcp_iflag_f32_e32 v7, v8
	v_ashrrev_i32_e32 v8, 31, v3
	s_ashr_i32 s3, s3, 31
	v_xor_b32_e32 v9, s3, v8
	v_mul_f32_e32 v7, 0x4f7ffffe, v7
	v_cvt_u32_f32_e32 v7, v7
	s_sub_i32 s3, 0, s5
	v_sub_u32_e32 v11, 0, v3
	v_max_i32_e32 v11, v3, v11
	v_mul_lo_u32 v12, s3, v7
	v_mul_hi_u32 v12, v7, v12
	v_add_u32_e32 v7, v7, v12
	v_mul_hi_u32 v7, v11, v7
	v_mul_lo_u32 v12, v7, s5
	v_sub_u32_e32 v12, v11, v12
	v_add_u32_e32 v13, 1, v7
	v_cmp_le_u32_e32 vcc, s5, v12
	s_abs_i32 s3, s8
	v_cvt_f32_u32_e32 v14, s3
	v_cndmask_b32_e32 v7, v7, v13, vcc
	v_subrev_u32_e32 v13, s5, v12
	v_cndmask_b32_e32 v12, v12, v13, vcc
	v_add_u32_e32 v13, 1, v7
	v_cmp_le_u32_e32 vcc, s5, v12
	s_sub_i32 s5, 0, s3
	v_lshl_or_b32 v1, v6, 5, v1
	v_cndmask_b32_e32 v7, v7, v13, vcc
	v_xor_b32_e32 v7, v7, v9
	v_sub_u32_e32 v7, v7, v9
	v_rcp_iflag_f32_e32 v9, v14
	v_mul_lo_u32 v12, v7, s4
	v_sub_u32_e32 v13, 0, v7
	v_sub_u32_e32 v3, v3, v12
	v_mul_f32_e32 v9, 0x4f7ffffe, v9
	v_cvt_u32_f32_e32 v9, v9
	v_ashrrev_i32_e32 v12, 31, v7
	v_max_i32_e32 v7, v7, v13
	s_mul_i32 s4, s4, s8
	v_mul_lo_u32 v13, s5, v9
	v_mul_hi_u32 v13, v9, v13
	v_add_u32_e32 v9, v9, v13
	s_abs_i32 s5, s4
	v_mul_hi_u32 v9, v7, v9
	v_cvt_f32_u32_e32 v13, s5
	v_mul_lo_u32 v9, v9, s3
	v_sub_u32_e32 v7, v7, v9
	v_subrev_u32_e32 v9, s3, v7
	v_cmp_le_u32_e32 vcc, s3, v7
	v_rcp_iflag_f32_e32 v13, v13
	v_lshl_or_b32 v6, v3, 4, v10
	v_cndmask_b32_e32 v7, v7, v9, vcc
	v_subrev_u32_e32 v9, s3, v7
	v_cmp_le_u32_e32 vcc, s3, v7
	s_ashr_i32 s3, s4, 31
	v_xor_b32_e32 v8, s3, v8
	v_cndmask_b32_e32 v7, v7, v9, vcc
	v_xor_b32_e32 v7, v7, v12
	v_sub_u32_e32 v12, v7, v12
	v_mul_f32_e32 v7, 0x4f7ffffe, v13
	v_cvt_u32_f32_e32 v7, v7
	s_sub_i32 s3, 0, s5
	v_ashrrev_i32_e32 v13, 31, v12
	v_lshl_add_u64 v[4:5], v[12:13], 2, v[4:5]
	v_mul_lo_u32 v9, s3, v7
	v_mul_hi_u32 v9, v7, v9
	v_add_u32_e32 v7, v7, v9
	v_mul_hi_u32 v7, v11, v7
	v_mul_lo_u32 v9, v7, s5
	v_sub_u32_e32 v9, v11, v9
	v_add_u32_e32 v11, 1, v7
	v_cmp_le_u32_e32 vcc, s5, v9
	s_ashr_i32 s3, s8, 31
	v_mov_b32_e32 v3, 0
	v_cndmask_b32_e32 v7, v7, v11, vcc
	v_subrev_u32_e32 v11, s5, v9
	v_cndmask_b32_e32 v9, v9, v11, vcc
	v_add_u32_e32 v11, 1, v7
	v_cmp_le_u32_e32 vcc, s5, v9
	s_nop 1
	v_cndmask_b32_e32 v7, v7, v11, vcc
	v_xor_b32_e32 v7, v7, v8
	v_sub_u32_e32 v7, v7, v8
	v_cmp_gt_i32_e32 vcc, s10, v1
	v_mad_u64_u32 v[8:9], s[4:5], v7, s16, v[6:7]
	v_mad_i64_i32 v[6:7], s[4:5], v1, s9, 0
	v_mov_b32_e32 v1, 0
	s_and_saveexec_b64 s[4:5], vcc
	s_cbranch_execz .LBB0_101
	v_ashrrev_i32_e32 v9, 31, v8
	v_lshl_add_u64 v[10:11], v[6:7], 0, v[8:9]
	v_mul_lo_u32 v1, v11, s8
	v_mul_lo_u32 v9, v10, s3
	v_mad_u64_u32 v[10:11], s[10:11], v10, s8, 0
	v_add3_u32 v11, v11, v9, v1
	v_lshl_add_u64 v[10:11], v[10:11], 2, v[4:5]
	global_load_dword v1, v[10:11], off
.LBB0_101:
	s_or_b64 exec, exec, s[4:5]
	s_and_saveexec_b64 s[4:5], vcc
	s_cbranch_execz .LBB0_103
	v_add_u32_e32 v10, 1, v8
	v_ashrrev_i32_e32 v11, 31, v10
	v_lshl_add_u64 v[10:11], v[6:7], 0, v[10:11]
	v_mul_lo_u32 v3, v11, s8
	v_mul_lo_u32 v9, v10, s3
	v_mad_u64_u32 v[10:11], s[10:11], v10, s8, 0
	v_add3_u32 v11, v11, v9, v3
	v_lshl_add_u64 v[10:11], v[10:11], 2, v[4:5]
	global_load_dword v3, v[10:11], off
.LBB0_103:
	s_or_b64 exec, exec, s[4:5]
	v_mov_b32_e32 v9, 0
	v_mov_b32_e32 v10, 0
	s_and_saveexec_b64 s[4:5], vcc
	s_cbranch_execz .LBB0_105
	v_add_u32_e32 v10, 2, v8
	v_ashrrev_i32_e32 v11, 31, v10
	v_lshl_add_u64 v[10:11], v[6:7], 0, v[10:11]
	v_mul_lo_u32 v12, v11, s8
	v_mul_lo_u32 v13, v10, s3
	v_mad_u64_u32 v[10:11], s[10:11], v10, s8, 0
	v_add3_u32 v11, v11, v13, v12
	v_lshl_add_u64 v[10:11], v[10:11], 2, v[4:5]
	global_load_dword v10, v[10:11], off
.LBB0_105:
	s_or_b64 exec, exec, s[4:5]
	s_and_saveexec_b64 s[4:5], vcc
	s_cbranch_execz .LBB0_107
	v_add_u32_e32 v12, 3, v8
	v_ashrrev_i32_e32 v13, 31, v12
	v_lshl_add_u64 v[12:13], v[6:7], 0, v[12:13]
	v_mul_lo_u32 v9, v13, s8
	v_mul_lo_u32 v11, v12, s3
	v_mad_u64_u32 v[12:13], s[10:11], v12, s8, 0
	v_add3_u32 v13, v13, v11, v9
	v_lshl_add_u64 v[12:13], v[12:13], 2, v[4:5]
	global_load_dword v9, v[12:13], off
.LBB0_107:
	s_or_b64 exec, exec, s[4:5]
	v_mov_b32_e32 v11, 0
	v_mov_b32_e32 v12, 0
	s_and_saveexec_b64 s[4:5], vcc
	s_cbranch_execz .LBB0_109
	v_add_u32_e32 v12, 4, v8
	v_ashrrev_i32_e32 v13, 31, v12
	v_lshl_add_u64 v[12:13], v[6:7], 0, v[12:13]
	v_mul_lo_u32 v14, v13, s8
	v_mul_lo_u32 v15, v12, s3
	v_mad_u64_u32 v[12:13], s[10:11], v12, s8, 0
	v_add3_u32 v13, v13, v15, v14
	v_lshl_add_u64 v[12:13], v[12:13], 2, v[4:5]
	global_load_dword v12, v[12:13], off
.LBB0_109:
	s_or_b64 exec, exec, s[4:5]
	s_and_saveexec_b64 s[4:5], vcc
	s_cbranch_execz .LBB0_111
	v_add_u32_e32 v14, 5, v8
	v_ashrrev_i32_e32 v15, 31, v14
	v_lshl_add_u64 v[14:15], v[6:7], 0, v[14:15]
	v_mul_lo_u32 v11, v15, s8
	v_mul_lo_u32 v13, v14, s3
	v_mad_u64_u32 v[14:15], s[10:11], v14, s8, 0
	v_add3_u32 v15, v15, v13, v11
	v_lshl_add_u64 v[14:15], v[14:15], 2, v[4:5]
	global_load_dword v11, v[14:15], off
.LBB0_111:
	s_or_b64 exec, exec, s[4:5]
	v_mov_b32_e32 v13, 0
	v_mov_b32_e32 v14, 0
	s_and_saveexec_b64 s[4:5], vcc
	s_cbranch_execz .LBB0_113
	v_add_u32_e32 v14, 6, v8
	v_ashrrev_i32_e32 v15, 31, v14
	v_lshl_add_u64 v[14:15], v[6:7], 0, v[14:15]
	v_mul_lo_u32 v16, v15, s8
	v_mul_lo_u32 v17, v14, s3
	v_mad_u64_u32 v[14:15], s[10:11], v14, s8, 0
	v_add3_u32 v15, v15, v17, v16
	v_lshl_add_u64 v[14:15], v[14:15], 2, v[4:5]
	global_load_dword v14, v[14:15], off
.LBB0_113:
	s_or_b64 exec, exec, s[4:5]
	s_and_saveexec_b64 s[4:5], vcc
	s_cbranch_execz .LBB0_115
	v_add_u32_e32 v16, 7, v8
	v_ashrrev_i32_e32 v17, 31, v16
	v_lshl_add_u64 v[6:7], v[6:7], 0, v[16:17]
	v_mul_lo_u32 v8, v7, s8
	v_mul_lo_u32 v13, v6, s3
	v_mad_u64_u32 v[6:7], s[8:9], v6, s8, 0
	v_add3_u32 v7, v7, v13, v8
	v_lshl_add_u64 v[4:5], v[6:7], 2, v[4:5]
	global_load_dword v13, v[4:5], off
.LBB0_115:
	s_or_b64 exec, exec, s[4:5]
	s_waitcnt vmcnt(0)
	v_mul_f32_e32 v1, 0x42800000, v1
	v_mul_f32_e32 v3, 0x42800000, v3
	v_mul_f32_e32 v10, 0x42800000, v10
	v_mul_f32_e32 v9, 0x42800000, v9
	v_mul_f32_e32 v12, 0x42800000, v12
	v_mul_f32_e32 v11, 0x42800000, v11
	v_mul_f32_e32 v14, 0x42800000, v14
	v_mul_f32_e32 v13, 0x42800000, v13
	v_cvt_f16_f32_e32 v4, v1
	v_cvt_f16_f32_e32 v5, v3
	v_cvt_f16_f32_e32 v6, v10
	v_cvt_f16_f32_e32 v7, v9
	v_cvt_f32_f16_e32 v4, v4
	v_cvt_f32_f16_e32 v5, v5
	v_cvt_f32_f16_e32 v6, v6
	v_sub_f32_e32 v8, v1, v4
	v_cvt_f16_f32_e32 v4, v12
	v_sub_f32_e32 v15, v3, v5
	v_sub_f32_e32 v16, v10, v6
	v_cvt_f32_f16_e32 v5, v7
	v_cvt_f16_f32_e32 v6, v11
	v_cvt_f16_f32_e32 v7, v14
	v_cvt_f32_f16_e32 v4, v4
	v_sub_f32_e32 v17, v9, v5
	v_cvt_f32_f16_e32 v5, v6
	v_cvt_f32_f16_e32 v6, v7
	v_sub_f32_e32 v18, v12, v4
	v_cvt_f16_f32_e32 v4, v13
	v_cvt_pk_f16_f32 v7, v14, v13
	v_sub_f32_e32 v20, v14, v6
	v_sub_f32_e32 v19, v11, v5
	v_cvt_f32_f16_e32 v14, v4
	v_cvt_pk_f16_f32 v4, v1, v3
	v_ashrrev_i32_e32 v3, 31, v2
	v_lshlrev_b64 v[2:3], 5, v[2:3]
	v_cvt_pk_f16_f32 v6, v12, v11
	v_cvt_pk_f16_f32 v5, v10, v9
	v_sub_f32_e32 v1, v13, v14
	v_lshl_add_u64 v[2:3], s[6:7], 0, v[2:3]
	v_cvt_pk_f16_f32 v11, v20, v1
	v_cvt_pk_f16_f32 v10, v18, v19
	v_cvt_pk_f16_f32 v9, v16, v17
	v_cvt_pk_f16_f32 v8, v8, v15
	global_store_dwordx4 v[2:3], v[4:7], off
	global_store_dwordx4 v[2:3], v[8:11], off offset:16

.LBB0_124:
	s_and_b64 vcc, exec, s[4:5]
	s_cbranch_vccz .LBB0_146
	s_load_dwordx8 s[16:23], s[0:1], 0xc8
	s_load_dwordx4 s[24:27], s[0:1], 0xe8
	s_ashr_i32 s3, s2, 31
	s_mul_i32 s0, s2, 0x1200
	s_mul_hi_i32 s1, s2, 0x1200
	s_waitcnt lgkmcnt(0)
	s_load_dword s30, s[20:21], 0x0
	s_load_dword s30, s[20:21], 0x40
	s_load_dword s30, s[20:21], 0x80
	s_load_dword s30, s[20:21], 0xc0
	s_load_dword s30, s[20:21], 0x100
	s_load_dword s30, s[20:21], 0x140
	s_load_dword s30, s[20:21], 0x180
	s_load_dword s30, s[20:21], 0x1c0
	s_lshl_b32 s31, s2, 2
	s_load_dword s30, s[22:23], s31
	s_add_u32 s0, s16, s0
	v_lshlrev_b32_e32 v2, 2, v0
	v_mov_b32_e32 v3, 0
	s_addc_u32 s1, s17, s1
	v_or_b32_e32 v1, 0xffffff00, v0
	v_lshl_add_u64 v[4:5], s[0:1], 0, v[2:3]
	v_or_b32_e32 v3, 0x8000, v2
	s_mov_b64 s[0:1], 0
	s_mov_b64 s[4:5], 0x400
	s_movk_i32 s6, 0x37f
.LBB0_126:
	global_load_dword v6, v[4:5], off
	global_load_dword v20, v[4:5], off offset:1024
	global_load_dword v21, v[4:5], off offset:2048
	global_load_dword v22, v[4:5], off offset:3072
	v_add_co_u32_e32 v24, vcc, 0x1000, v4
	s_nop 1
	v_addc_co_u32_e32 v25, vcc, 0, v5, vcc
	v_cmp_gt_u32_e32 vcc, 0x80, v0
	s_nop 1
	s_and_saveexec_b64 s[0:1], vcc
	global_load_dword v23, v[24:25], off
	s_or_b64 exec, exec, s[0:1]
	s_waitcnt vmcnt(0) lgkmcnt(0)
	ds_write_b32 v3, v6
	ds_write_b32 v3, v20 offset:1024
	ds_write_b32 v3, v21 offset:2048
	ds_write_b32 v3, v22 offset:3072
	s_and_saveexec_b64 s[0:1], vcc
	ds_write_b32 v3, v23 offset:4096
	s_or_b64 exec, exec, s[0:1]
	s_mov_b64 s[0:1], 0
	s_or_b64 exec, exec, s[0:1]
	v_or_b32_e32 v1, 0x100, v0
	v_mov_b32_e32 v8, 16
	s_mov_b64 s[0:1], 0
	v_mov_b32_e32 v7, 0
	v_mov_b32_e32 v3, v2
	v_mov_b64_e32 v[4:5], v[0:1]
